# v33: v21 + scatter table copies batched + MoE gate/up next-tile lookups in one round trip
# speedup vs baseline: 1.0090x; 1.0022x over previous
.LBB0_1722:
	v_cndmask_b32_e64 v130, 0, 1, s[50:51]
	v_cmp_ne_u32_e64 s[2:3], 1, v130
	s_andn2_b64 vcc, exec, s[50:51]
	s_mov_b64 s[50:51], s[22:23]
	v_mov_b32_e32 v173, v175
	v_mov_b32_e32 v169, v172
	v_mov_b32_e32 v170, v174
	v_mov_b32_e32 v168, v171
	s_cbranch_vccnz .LBB0_1728
	s_and_b64 vcc, exec, s[38:39]
	s_cbranch_vccnz .LBB0_1725
	s_ashr_i32 s45, s44, 31
	s_cmp_eq_u32 s44, s101
	s_cbranch_scc1 .Lgu_texp_hit
	s_lshl_b64 s[0:1], s[44:45], 2
	s_add_u32 s0, s40, s0
	s_addc_u32 s1, s41, s1
	s_cmp_eq_u32 s44, s48
	s_cbranch_scc0 .Lgu_comb
	global_load_dword v130, v203, s[0:1]
	s_waitcnt vmcnt(0)
	v_readfirstlane_b32 s100, v130
	s_mov_b32 s101, s44

.Lgu_comb:
	global_load_dword v145, v203, s[0:1]
	v_mov_b32_e32 v130, v1
	s_lshl_b32 s0, s44, 8
	s_or_b32 s1, s0, 0x80
	v_ashrrev_i32_e32 v131, 31, v130
	v_lshrrev_b32_e32 v131, 26, v131
	v_lshlrev_b32_e32 v132, 4, v130
	v_add_u32_e32 v131, v130, v131
	v_bfe_i32 v130, v130, 27, 1
	v_lshrrev_b32_e32 v130, 22, v130
	v_add_u32_e32 v130, v132, v130
	v_and_b32_e32 v130, 0xfffffc00, v130
	v_sub_u32_e32 v130, v132, v130
	v_lshrrev_b32_e32 v133, 4, v130
	v_bitop3_b32 v130, v133, v130, 32 bitop3:0x6c
	v_ashrrev_i32_e32 v134, 31, v130
	v_lshrrev_b32_e32 v134, 26, v134
	v_add_u32_e32 v134, v130, v134
	v_ashrrev_i32_e32 v131, 6, v131
	v_ashrrev_i32_e32 v135, 6, v134
	v_and_b32_e32 v134, 0xc0, v134
	v_lshlrev_b32_e32 v133, 3, v131
	v_sub_u32_e32 v130, v130, v134
	v_and_b32_e32 v133, -16, v133
	v_lshlrev_b32_e32 v131, 5, v131
	v_ashrrev_i16_sdwa v130, v217, sext(v130) dst_sel:DWORD dst_unused:UNUSED_PAD src0_sel:DWORD src1_sel:BYTE_0
	v_and_b32_e32 v131, 32, v131
	v_bfe_i32 v130, v130, 0, 16
	v_add_u32_e32 v133, v135, v133
	v_add_lshl_u32 v134, v131, v130, 1
	v_add_u32_e32 v130, s0, v133
	v_ashrrev_i32_e32 v131, 31, v130
	v_lshl_add_u64 v[130:131], v[130:131], 2, s[26:27]
	global_load_dword v136, v[130:131], off
	v_add_u32_e32 v130, s1, v133
	v_ashrrev_i32_e32 v131, 31, v130
	v_lshl_add_u64 v[130:131], v[130:131], 2, s[26:27]
	global_load_dword v137, v[130:131], off
	v_add_u32_e32 v140, 0x2000, v132
	v_ashrrev_i32_e32 v141, 31, v140
	v_lshrrev_b32_e32 v141, 22, v141
	v_add_u32_e32 v141, v140, v141
	v_ashrrev_i32_e32 v141, 10, v141
	v_mul_i32_i24_e32 v142, 0x400, v141
	v_sub_u32_e32 v140, v140, v142
	v_lshrrev_b32_e32 v142, 4, v140
	v_bitop3_b32 v140, v142, v140, 32 bitop3:0x6c
	v_ashrrev_i32_e32 v143, 31, v140
	v_lshrrev_b32_e32 v143, 26, v143
	v_add_u32_e32 v143, v140, v143
	v_ashrrev_i32_e32 v144, 6, v143
	v_and_b32_e32 v143, 0xc0, v143
	v_lshlrev_b32_e32 v142, 3, v141
	v_sub_u32_e32 v140, v140, v143
	v_and_b32_e32 v142, -16, v142
	v_lshlrev_b32_e32 v141, 5, v141
	v_ashrrev_i16_sdwa v140, v217, sext(v140) dst_sel:DWORD dst_unused:UNUSED_PAD src0_sel:DWORD src1_sel:BYTE_0
	v_and_b32_e32 v141, 32, v141
	v_bfe_i32 v140, v140, 0, 16
	v_add_u32_e32 v142, v144, v142
	v_add_lshl_u32 v143, v141, v140, 1
	v_add_u32_e32 v140, s0, v142
	v_ashrrev_i32_e32 v141, 31, v140
	v_lshl_add_u64 v[140:141], v[140:141], 2, s[26:27]
	global_load_dword v138, v[140:141], off
	v_add_u32_e32 v140, s1, v142
	v_ashrrev_i32_e32 v141, 31, v140
	v_lshl_add_u64 v[140:141], v[140:141], 2, s[26:27]
	global_load_dword v139, v[140:141], off
	s_waitcnt vmcnt(0)
	v_readfirstlane_b32 s100, v145
	s_mov_b32 s101, s44
	v_max_i32_e32 v136, 0, v136
	v_max_i32_e32 v137, 0, v137
	v_max_i32_e32 v138, 0, v138
	v_max_i32_e32 v139, 0, v139
	v_lshl_add_u32 v168, v136, 10, v134
	v_lshl_add_u32 v169, v137, 10, v134
	v_lshl_add_u32 v170, v138, 10, v143
	v_lshl_add_u32 v173, v139, 10, v143
	s_mul_hi_i32 s51, s100, 0x700000
	s_mul_i32 s50, s100, 0x700000
	s_add_u32 s16, s61, s50
	s_addc_u32 s17, s62, s51
	s_ashr_i32 s43, s42, 31
	s_lshl_b64 s[0:1], s[42:43], 18
	s_add_u32 s50, s16, s0
	s_addc_u32 s51, s17, s1
	s_branch .LBB0_1728
